# v39 + DSA selection-mask table addresses via one SDWA op per read (12 VALU per step instead of 18)
# baseline (speedup 1.0000x reference)
.LBB0_1066:
	s_andn2_b64 vcc, exec, s[0:1]
	s_cbranch_vccnz .LBB0_1165
	v_readlane_b32 s0, v250, 19
	v_readlane_b32 s1, v250, 20
	s_andn2_b64 vcc, exec, s[0:1]
	s_cbranch_vccnz .LBB0_1165
	s_add_u32 s0, s74, 0x7800000
	v_writelane_b32 v253, s0, 47
	s_addc_u32 s0, s75, 0
	v_writelane_b32 v253, s0, 49
	s_add_u32 s0, s74, 0xa800000
	v_writelane_b32 v253, s0, 50
	s_addc_u32 s0, s75, 0
	v_writelane_b32 v253, s0, 52
	s_add_u32 s0, s74, 0xb800000
	v_writelane_b32 v253, s0, 53
	s_addc_u32 s0, s75, 0
	s_waitcnt vmcnt(0) lgkmcnt(0)
	v_lshrrev_b32_e32 v3, 5, v198
	v_lshlrev_b32_e32 v4, 1, v235
	v_writelane_b32 v253, s0, 55
	s_add_u32 s0, s74, 0xeb00000
	v_and_b32_e32 v6, 32, v4
	v_lshlrev_b32_e32 v238, 2, v3
	v_lshrrev_b32_e32 v4, 2, v235
	s_addc_u32 s82, s75, 0
	v_and_b32_e32 v236, 31, v235
	v_and_or_b32 v4, v4, 3, v238
	v_writelane_b32 v253, s0, 57
	s_add_u32 s83, s74, 0xf0000
	v_lshlrev_b32_e32 v5, 3, v235
	v_lshlrev_b32_e32 v7, 6, v4
	v_lshlrev_b32_e32 v8, 4, v236
	v_lshlrev_b32_e32 v4, 9, v236
	s_addc_u32 s84, s75, 0
	v_and_b32_e32 v2, 24, v5
	v_lshl_or_b32 v4, v3, 3, v4
	v_lshl_or_b32 v241, v3, 10, v8
	v_lshlrev_b32_e32 v242, 9, v3
	v_lshrrev_b32_e32 v3, 3, v198
	v_readlane_b32 s0, v253, 4
	v_or3_b32 v239, v6, v2, v7
	v_and_b32_e32 v6, 56, v5
	v_or_b32_e32 v5, 8, v3
	s_add_u32 s85, s0, s86
	v_readlane_b32 s0, v253, 5
	v_lshlrev_b32_e32 v243, 7, v3
	v_lshlrev_b32_e32 v8, 9, v3
	v_lshlrev_b32_e32 v244, 7, v5
	v_lshlrev_b32_e32 v10, 9, v5
	v_or_b32_e32 v5, 16, v3
	v_or_b32_e32 v3, 24, v3
	s_addc_u32 s88, s0, s87
	v_readlane_b32 s0, v253, 6
	v_lshlrev_b32_e32 v0, 9, v198
	v_lshlrev_b32_e32 v12, 9, v5
	v_lshlrev_b32_e32 v14, 9, v3
	s_add_u32 s89, s0, s86
	v_readlane_b32 s0, v253, 7
	v_lshrrev_b32_e32 v237, 2, v198
	v_or_b32_e32 v240, 0x6000, v239
	v_cmp_gt_u32_e64 s[36:37], 32, v198
	v_lshlrev_b32_e32 v245, 7, v5
	v_lshlrev_b32_e32 v246, 7, v3
	s_addc_u32 s90, s0, s87
	v_lshlrev_b32_e32 v200, 1, v0
	v_lshlrev_b32_e32 v202, 1, v2
	v_lshlrev_b32_e32 v247, 1, v4
	v_lshlrev_b32_e32 v204, 1, v6
	v_lshlrev_b32_e32 v206, 1, v8
	v_lshlrev_b32_e32 v208, 1, v10
	v_lshlrev_b32_e32 v210, 1, v12
	v_lshlrev_b32_e32 v212, 1, v14
	v_readlane_b32 s91, v250, 9
	s_mov_b32 s100, 0x15000
	s_mov_b32 s101, 0xf0f0f0f0
	v_sub_u32_e32 v229, 4, v238
	v_lshrrev_b32_e32 v226, 2, v198
	v_and_b32_e32 v227, 3, v198
	v_lshrrev_b32_e32 v226, v227, v226
	v_and_b32_e32 v226, 1, v226
	v_cmp_eq_u32_e32 vcc, 1, v226
	v_mov_b32_e32 v226, 0xff800000
	s_nop 1
	v_cndmask_b32_e64 v226, v226, 0, vcc
	v_lshlrev_b32_e32 v227, 2, v198
	v_add_u32_e32 v227, s100, v227
	ds_write_b32 v227, v226
	s_waitcnt lgkmcnt(0)
	s_branch .LBB0_1070

.LBB0_1077:
	v_lshl_add_u64 v[14:15], v[184:185], 0, s[54:55]
	s_mov_b64 s[38:39], 0xeb20000
	v_lshl_add_u64 v[2:3], v[14:15], 0, s[38:39]
	s_mov_b64 s[38:39], 0xeb28000
	v_add_u32_e32 v12, s29, v239
	v_lshl_add_u64 v[4:5], v[14:15], 0, s[38:39]
	global_load_dword v0, v[2:3], off
	global_load_dword v190, v[4:5], off
	global_load_dword v191, v[182:183], off offset:-4
	v_lshlrev_b32_e32 v2, v229, v211
	v_lshlrev_b32_e32 v3, v229, v213
	v_and_b32_e32 v2, s101, v2
	v_and_b32_e32 v3, s101, v3
	v_or_b32_sdwa v4, v2, s100 dst_sel:DWORD dst_unused:UNUSED_PAD src0_sel:BYTE_0 src1_sel:DWORD
	ds_read_b128 v[80:83], v4
	v_or_b32_sdwa v4, v2, s100 dst_sel:DWORD dst_unused:UNUSED_PAD src0_sel:BYTE_1 src1_sel:DWORD
	ds_read_b128 v[84:87], v4
	v_or_b32_sdwa v4, v2, s100 dst_sel:DWORD dst_unused:UNUSED_PAD src0_sel:BYTE_2 src1_sel:DWORD
	ds_read_b128 v[88:91], v4
	v_or_b32_sdwa v4, v2, s100 dst_sel:DWORD dst_unused:UNUSED_PAD src0_sel:BYTE_3 src1_sel:DWORD
	ds_read_b128 v[92:95], v4
	v_or_b32_sdwa v4, v3, s100 dst_sel:DWORD dst_unused:UNUSED_PAD src0_sel:BYTE_0 src1_sel:DWORD
	ds_read_b128 v[96:99], v4
	v_or_b32_sdwa v4, v3, s100 dst_sel:DWORD dst_unused:UNUSED_PAD src0_sel:BYTE_1 src1_sel:DWORD
	ds_read_b128 v[100:103], v4
	v_or_b32_sdwa v4, v3, s100 dst_sel:DWORD dst_unused:UNUSED_PAD src0_sel:BYTE_2 src1_sel:DWORD
	ds_read_b128 v[104:107], v4
	v_or_b32_sdwa v4, v3, s100 dst_sel:DWORD dst_unused:UNUSED_PAD src0_sel:BYTE_3 src1_sel:DWORD
	ds_read_b128 v[108:111], v4
	ds_read_b64_tr_b16 v[176:177], v12 offset:24576
	ds_read_b64_tr_b16 v[178:179], v12 offset:25088
	s_waitcnt lgkmcnt(6)
	v_mfma_f32_32x32x16_bf16 v[80:95], v[172:175], v[124:127], v[80:95]
	v_add_f32_e32 v2, v64, v65
	v_add_f32_e32 v2, v66, v2
	v_add_f32_e32 v2, v67, v2
	v_add_f32_e32 v2, v68, v2
	v_add_f32_e32 v2, v69, v2
	v_cvt_pk_bf16_f32 v140, v64, v65
	v_cvt_pk_bf16_f32 v141, v66, v67
	ds_read_b64_tr_b16 v[172:173], v12 offset:28672
	ds_read_b64_tr_b16 v[174:175], v12 offset:29184
	s_waitcnt lgkmcnt(4)
	v_mfma_f32_32x32x16_bf16 v[96:111], v[164:167], v[124:127], v[96:111]
	v_add_f32_e32 v2, v70, v2
	v_add_f32_e32 v2, v71, v2
	v_add_f32_e32 v2, v72, v2
	v_add_f32_e32 v2, v73, v2
	v_cvt_pk_bf16_f32 v142, v68, v69
	v_cvt_pk_bf16_f32 v143, v70, v71
	ds_read_b64_tr_b16 v[164:165], v12 offset:25600
	ds_read_b64_tr_b16 v[166:167], v12 offset:26112
	v_mfma_f32_32x32x16_bf16 v[80:95], v[168:171], v[120:123], v[80:95]
	v_add_f32_e32 v2, v74, v2
	v_add_f32_e32 v2, v75, v2
	v_add_f32_e32 v2, v76, v2
	v_add_f32_e32 v2, v77, v2
	v_cvt_pk_bf16_f32 v136, v72, v73
	v_cvt_pk_bf16_f32 v137, v74, v75
	ds_read_b64_tr_b16 v[168:169], v12 offset:29696
	ds_read_b64_tr_b16 v[170:171], v12 offset:30208
	v_mfma_f32_32x32x16_bf16 v[96:111], v[160:163], v[120:123], v[96:111]
	v_add_f32_e32 v2, v78, v2
	v_add_f32_e32 v2, v79, v2
	v_add_f32_e32 v2, v48, v2
	v_add_f32_e32 v2, v49, v2
	v_cvt_pk_bf16_f32 v138, v76, v77
	v_cvt_pk_bf16_f32 v139, v78, v79
	ds_read_b64_tr_b16 v[160:161], v12 offset:26624
	ds_read_b64_tr_b16 v[162:163], v12 offset:27136
	v_mfma_f32_32x32x16_bf16 v[80:95], v[156:159], v[116:119], v[80:95]
	v_add_f32_e32 v2, v50, v2
	v_add_f32_e32 v2, v51, v2
	v_add_f32_e32 v2, v52, v2
	v_add_f32_e32 v6, v53, v2
	v_cvt_pk_bf16_f32 v132, v48, v49
	v_cvt_pk_bf16_f32 v133, v50, v51
	ds_read_b64_tr_b16 v[2:3], v12 offset:30720
	ds_read_b64_tr_b16 v[4:5], v12 offset:31232
	v_mfma_f32_32x32x16_bf16 v[96:111], v[152:155], v[116:119], v[96:111]
	v_add_f32_e32 v6, v54, v6
	v_add_f32_e32 v6, v55, v6
	v_add_f32_e32 v6, v56, v6
	v_add_f32_e32 v10, v57, v6
	v_cvt_pk_bf16_f32 v134, v52, v53
	v_cvt_pk_bf16_f32 v135, v54, v55
	ds_read_b64_tr_b16 v[6:7], v12 offset:27648
	ds_read_b64_tr_b16 v[8:9], v12 offset:28160
	v_mfma_f32_32x32x16_bf16 v[80:95], v[148:151], v[112:115], v[80:95]
	v_add_f32_e32 v10, v58, v10
	v_add_f32_e32 v10, v59, v10
	v_add_f32_e32 v10, v60, v10
	v_add_f32_e32 v48, v61, v10
	v_cvt_pk_bf16_f32 v128, v56, v57
	v_cvt_pk_bf16_f32 v129, v58, v59
	ds_read_b64_tr_b16 v[10:11], v12 offset:31744
	ds_read_b64_tr_b16 v[12:13], v12 offset:32256
	v_mfma_f32_32x32x16_bf16 v[96:111], v[144:147], v[112:115], v[96:111]
	v_add_f32_e32 v48, v62, v48
	v_add_f32_e32 v48, v63, v48
	v_cvt_pk_bf16_f32 v130, v60, v61
	v_cvt_pk_bf16_f32 v131, v62, v63
	v_lshl_add_u64 v[186:187], v[216:217], 0, s[54:55]
	v_lshl_add_u64 v[50:51], v[186:187], 0, s[20:21]
	s_add_i32 s29, s59, s63
	s_mov_b32 m0, s29
	s_nop 0
	global_load_lds_dwordx4 v[50:51], off
	v_lshl_add_u64 v[188:189], v[218:219], 0, s[54:55]
	v_lshl_add_u64 v[50:51], v[188:189], 0, s[24:25]
	s_add_i32 s29, s57, s62
	s_mov_b32 m0, s29
	s_nop 0
	global_load_lds_dwordx4 v[50:51], off
	s_waitcnt vmcnt(7)
	v_mul_f32_e32 v49, v201, v209
	v_cmp_nge_f32_e32 vcc, s73, v49
	v_cmp_neq_f32_e64 s[38:39], 0, v207
	s_or_b64 vcc, vcc, s[38:39]
	s_cmp_lg_u64 vcc, 0
	s_cselect_b64 s[38:39], -1, 0
	s_cbranch_vccz .LBB0_1079
	v_sub_f32_e32 v95, v95, v207
	v_sub_f32_e32 v94, v94, v207
	v_sub_f32_e32 v93, v93, v207
	v_sub_f32_e32 v92, v92, v207
	v_sub_f32_e32 v91, v91, v207
	v_sub_f32_e32 v90, v90, v207
	v_sub_f32_e32 v89, v89, v207
	v_sub_f32_e32 v88, v88, v207
	v_sub_f32_e32 v87, v87, v207
	v_sub_f32_e32 v86, v86, v207
	v_sub_f32_e32 v85, v85, v207
	v_sub_f32_e32 v84, v84, v207
	v_sub_f32_e32 v83, v83, v207
	v_sub_f32_e32 v82, v82, v207
	v_sub_f32_e32 v81, v81, v207
	v_sub_f32_e32 v80, v80, v207
	v_sub_f32_e32 v111, v111, v207
	v_sub_f32_e32 v110, v110, v207
	v_sub_f32_e32 v109, v109, v207
	v_sub_f32_e32 v108, v108, v207
	v_sub_f32_e32 v107, v107, v207
	v_sub_f32_e32 v106, v106, v207
	v_sub_f32_e32 v105, v105, v207
	v_sub_f32_e32 v104, v104, v207
	v_sub_f32_e32 v103, v103, v207
	v_sub_f32_e32 v102, v102, v207
	v_sub_f32_e32 v101, v101, v207
	v_sub_f32_e32 v100, v100, v207
	v_sub_f32_e32 v99, v99, v207
	v_sub_f32_e32 v98, v98, v207
	v_sub_f32_e32 v97, v97, v207
	v_sub_f32_e32 v96, v96, v207

.LBB0_1082:
	s_add_i32 s29, s57, 0x2000
	s_cmpk_lg_i32 s57, 0x4000
	s_cselect_b32 s65, s29, 0
	s_mov_b64 s[38:39], 0xeb30000
	v_add_u32_e32 v12, s59, v239
	v_lshl_add_u64 v[2:3], v[14:15], 0, s[38:39]
	global_load_dword v192, v[2:3], off
	s_mov_b64 s[38:39], 0xeb38000
	v_lshl_add_u64 v[2:3], v[14:15], 0, s[38:39]
	global_load_dword v14, v[2:3], off
	global_load_dword v209, v[182:183], off
	v_lshlrev_b32_e32 v2, v229, v0
	v_lshlrev_b32_e32 v3, v229, v190
	v_and_b32_e32 v2, s101, v2
	v_and_b32_e32 v3, s101, v3
	v_or_b32_sdwa v4, v2, s100 dst_sel:DWORD dst_unused:UNUSED_PAD src0_sel:BYTE_0 src1_sel:DWORD
	ds_read_b128 v[80:83], v4
	v_or_b32_sdwa v4, v2, s100 dst_sel:DWORD dst_unused:UNUSED_PAD src0_sel:BYTE_1 src1_sel:DWORD
	ds_read_b128 v[84:87], v4
	v_or_b32_sdwa v4, v2, s100 dst_sel:DWORD dst_unused:UNUSED_PAD src0_sel:BYTE_2 src1_sel:DWORD
	ds_read_b128 v[88:91], v4
	v_or_b32_sdwa v4, v2, s100 dst_sel:DWORD dst_unused:UNUSED_PAD src0_sel:BYTE_3 src1_sel:DWORD
	ds_read_b128 v[92:95], v4
	v_or_b32_sdwa v4, v3, s100 dst_sel:DWORD dst_unused:UNUSED_PAD src0_sel:BYTE_0 src1_sel:DWORD
	ds_read_b128 v[96:99], v4
	v_or_b32_sdwa v4, v3, s100 dst_sel:DWORD dst_unused:UNUSED_PAD src0_sel:BYTE_1 src1_sel:DWORD
	ds_read_b128 v[100:103], v4
	v_or_b32_sdwa v4, v3, s100 dst_sel:DWORD dst_unused:UNUSED_PAD src0_sel:BYTE_2 src1_sel:DWORD
	ds_read_b128 v[104:107], v4
	v_or_b32_sdwa v4, v3, s100 dst_sel:DWORD dst_unused:UNUSED_PAD src0_sel:BYTE_3 src1_sel:DWORD
	ds_read_b128 v[108:111], v4
	ds_read_b64_tr_b16 v[156:157], v12 offset:24576
	ds_read_b64_tr_b16 v[158:159], v12 offset:25088
	s_waitcnt lgkmcnt(6)
	v_mfma_f32_32x32x16_bf16 v[80:95], v[140:143], v[124:127], v[80:95]
	v_add_f32_e32 v2, v64, v65
	v_add_f32_e32 v2, v66, v2
	v_add_f32_e32 v2, v67, v2
	v_add_f32_e32 v2, v68, v2
	v_add_f32_e32 v2, v69, v2
	v_cvt_pk_bf16_f32 v140, v64, v65
	v_cvt_pk_bf16_f32 v141, v66, v67
	ds_read_b64_tr_b16 v[152:153], v12 offset:28672
	ds_read_b64_tr_b16 v[154:155], v12 offset:29184
	s_waitcnt lgkmcnt(4)
	v_mfma_f32_32x32x16_bf16 v[96:111], v[136:139], v[124:127], v[96:111]
	v_add_f32_e32 v2, v70, v2
	v_add_f32_e32 v2, v71, v2
	v_add_f32_e32 v2, v72, v2
	v_add_f32_e32 v2, v73, v2
	v_cvt_pk_bf16_f32 v142, v68, v69
	v_cvt_pk_bf16_f32 v143, v70, v71
	ds_read_b64_tr_b16 v[144:145], v12 offset:25600
	ds_read_b64_tr_b16 v[146:147], v12 offset:26112
	v_mfma_f32_32x32x16_bf16 v[80:95], v[148:151], v[120:123], v[80:95]
	v_add_f32_e32 v2, v74, v2
	v_add_f32_e32 v2, v75, v2
	v_add_f32_e32 v2, v76, v2
	v_add_f32_e32 v2, v77, v2
	v_cvt_pk_bf16_f32 v136, v72, v73
	v_cvt_pk_bf16_f32 v137, v74, v75
	ds_read_b64_tr_b16 v[148:149], v12 offset:29696
	ds_read_b64_tr_b16 v[150:151], v12 offset:30208
	v_mfma_f32_32x32x16_bf16 v[96:111], v[176:179], v[120:123], v[96:111]
	v_add_f32_e32 v2, v78, v2
	v_add_f32_e32 v2, v79, v2
	v_add_f32_e32 v2, v48, v2
	v_add_f32_e32 v2, v49, v2
	v_cvt_pk_bf16_f32 v138, v76, v77
	v_cvt_pk_bf16_f32 v139, v78, v79
	ds_read_b64_tr_b16 v[176:177], v12 offset:26624
	ds_read_b64_tr_b16 v[178:179], v12 offset:27136
	v_mfma_f32_32x32x16_bf16 v[80:95], v[172:175], v[116:119], v[80:95]
	v_add_f32_e32 v2, v50, v2
	v_add_f32_e32 v2, v51, v2
	v_add_f32_e32 v2, v52, v2
	v_add_f32_e32 v6, v53, v2
	v_cvt_pk_bf16_f32 v132, v48, v49
	v_cvt_pk_bf16_f32 v133, v50, v51
	ds_read_b64_tr_b16 v[2:3], v12 offset:30720
	ds_read_b64_tr_b16 v[4:5], v12 offset:31232
	v_mfma_f32_32x32x16_bf16 v[96:111], v[164:167], v[116:119], v[96:111]
	v_add_f32_e32 v6, v54, v6
	v_add_f32_e32 v6, v55, v6
	v_add_f32_e32 v6, v56, v6
	v_add_f32_e32 v10, v57, v6
	v_cvt_pk_bf16_f32 v134, v52, v53
	v_cvt_pk_bf16_f32 v135, v54, v55
	ds_read_b64_tr_b16 v[6:7], v12 offset:27648
	ds_read_b64_tr_b16 v[8:9], v12 offset:28160
	v_mfma_f32_32x32x16_bf16 v[80:95], v[168:171], v[112:115], v[80:95]
	v_add_f32_e32 v10, v58, v10
	v_add_f32_e32 v10, v59, v10
	v_add_f32_e32 v10, v60, v10
	v_add_f32_e32 v15, v61, v10
	v_cvt_pk_bf16_f32 v128, v56, v57
	v_cvt_pk_bf16_f32 v129, v58, v59
	ds_read_b64_tr_b16 v[10:11], v12 offset:31744
	ds_read_b64_tr_b16 v[12:13], v12 offset:32256
	v_mfma_f32_32x32x16_bf16 v[96:111], v[160:163], v[112:115], v[96:111]
	v_add_f32_e32 v15, v62, v15
	v_add_f32_e32 v15, v63, v15
	v_cvt_pk_bf16_f32 v130, v60, v61
	v_cvt_pk_bf16_f32 v131, v62, v63
	v_lshl_add_u64 v[48:49], v[186:187], 0, s[22:23]
	s_add_i32 s29, s57, s63
	s_mov_b32 m0, s29
	s_nop 0
	global_load_lds_dwordx4 v[48:49], off
	v_lshl_add_u64 v[48:49], v[188:189], 0, s[70:71]
	s_add_i32 s29, s65, s62
	s_mov_b32 m0, s29
	s_nop 0
	global_load_lds_dwordx4 v[48:49], off
	s_waitcnt vmcnt(7)
	v_mul_f32_e32 v48, v201, v191
	v_cmp_nge_f32_e32 vcc, s73, v48
	v_cmp_neq_f32_e64 s[38:39], 0, v207
	s_or_b64 vcc, vcc, s[38:39]
	s_cmp_lg_u64 vcc, 0
	s_cselect_b64 s[38:39], -1, 0
	s_cbranch_vccz .LBB0_1084
	v_sub_f32_e32 v95, v95, v207
	v_sub_f32_e32 v94, v94, v207
	v_sub_f32_e32 v93, v93, v207
	v_sub_f32_e32 v92, v92, v207
	v_sub_f32_e32 v91, v91, v207
	v_sub_f32_e32 v90, v90, v207
	v_sub_f32_e32 v89, v89, v207
	v_sub_f32_e32 v88, v88, v207
	v_sub_f32_e32 v87, v87, v207
	v_sub_f32_e32 v86, v86, v207
	v_sub_f32_e32 v85, v85, v207
	v_sub_f32_e32 v84, v84, v207
	v_sub_f32_e32 v83, v83, v207
	v_sub_f32_e32 v82, v82, v207
	v_sub_f32_e32 v81, v81, v207
	v_sub_f32_e32 v80, v80, v207
	v_sub_f32_e32 v111, v111, v207
	v_sub_f32_e32 v110, v110, v207
	v_sub_f32_e32 v109, v109, v207
	v_sub_f32_e32 v108, v108, v207
	v_sub_f32_e32 v107, v107, v207
	v_sub_f32_e32 v106, v106, v207
	v_sub_f32_e32 v105, v105, v207
	v_sub_f32_e32 v104, v104, v207
	v_sub_f32_e32 v103, v103, v207
	v_sub_f32_e32 v102, v102, v207
	v_sub_f32_e32 v101, v101, v207
	v_sub_f32_e32 v100, v100, v207
	v_sub_f32_e32 v99, v99, v207
	v_sub_f32_e32 v98, v98, v207
	v_sub_f32_e32 v97, v97, v207
	v_sub_f32_e32 v96, v96, v207
